# speedup vs baseline: 1.0681x; 1.0075x over previous
_Z11attn_kernelPKfS0_S0_PKcS2_PKDv4_jS0_S0_S0_S0_Pf:
	s_load_dwordx8 s[4:11], s[0:1], 0x0
	s_load_dwordx8 s[12:19], s[0:1], 0x20
	v_readfirstlane_b32 s20, v0
	s_bfe_u32 s28, s2, 0x10002
	s_lshr_b32 s29, s20, 6
	s_lshr_b32 s3, s20, 8
	s_bfe_u32 s30, s20, 0x20006
	s_lshr_b32 s31, s2, 3
	s_lshl_b32 s24, s28, 18
	s_waitcnt lgkmcnt(0)
	s_add_u32 s20, s10, s24
	s_addc_u32 s10, s11, 0
	s_and_b32 s21, s10, 0xffff
	s_add_u32 s24, s12, s24
	s_addc_u32 s10, s13, 0
	v_and_b32_e32 v1, 63, v0
	s_and_b32 s25, s10, 0xffff
	s_lshl_b32 s10, s30, 10
	s_lshl_b32 s38, s3, 12
	v_lshlrev_b32_e32 v2, 4, v1
	s_or_b32 s35, s10, s38
	v_lshl_or_b32 v2, s3, 17, v2
	s_cmp_lg_u32 0, -1
	v_or_b32_e32 v174, s10, v2
	s_cselect_b32 s10, 0, 0
	s_mov_b32 s36, 0
	s_mov_b32 s23, 0x20000
	s_mov_b32 s22, 0x40000
	s_add_i32 s33, s35, s10
	s_mov_b32 m0, s33
	s_nop 0
	buffer_load_dwordx4 v174, s[20:23], s36 offen lds
	s_mov_b32 s26, s22
	s_mov_b32 s27, s23
	s_add_i32 s34, s33, 0xc000
	s_mov_b32 m0, s34
	s_nop 0
	buffer_load_dwordx4 v174, s[24:27], s36 offen lds
	s_add_i32 s10, s33, 0x4000
	s_movk_i32 s37, 0x1000
	s_mov_b32 m0, s10
	s_nop 0
	buffer_load_dwordx4 v174, s[20:23], s37 offen lds
	s_add_i32 s10, s33, 0x8000
	s_movk_i32 s11, 0x2000
	s_mov_b32 m0, s10
	s_nop 0
	buffer_load_dwordx4 v174, s[20:23], s11 offen lds
	s_lshl_b32 s10, s2, 7
	s_and_b32 s10, s10, 0x380
	s_lshl_b32 s11, s31, 2
	s_add_i32 s10, s10, s11
	s_or_b32 s10, s30, s10
	v_and_b32_e32 v172, 31, v0
	v_lshl_or_b32 v140, s10, 7, v1
	v_mov_b32_e32 v141, 0
	v_lshl_add_u64 v[6:7], v[140:141], 4, s[14:15]
	v_ashrrev_i32_e32 v9, 31, v140
	v_mov_b32_e32 v8, v140
	v_lshl_or_b32 v140, s10, 5, v172
	v_lshlrev_b64 v[4:5], 2, v[140:141]
	v_lshl_add_u64 v[2:3], s[16:17], 0, v[4:5]
	global_load_dword v2, v[2:3], off
	v_lshl_add_u64 v[8:9], v[8:9], 4, s[14:15]
	global_load_dwordx4 v[116:119], v[6:7], off
	global_load_dwordx4 v[120:123], v[8:9], off offset:1024
	s_load_dwordx4 s[12:15], s[0:1], 0x40
	s_load_dwordx2 s[10:11], s[0:1], 0x50
	v_lshlrev_b32_e32 v173, 2, v1
	v_lshl_or_b32 v3, s28, 11, v173
	s_waitcnt lgkmcnt(0)
	global_load_dword v44, v3, s[14:15] offset:256
	global_load_dword v45, v3, s[14:15]
	v_bfe_u32 v175, v0, 5, 1
	v_lshlrev_b32_e32 v0, 11, v175
	v_lshlrev_b32_e32 v3, 4, v172
	s_add_i32 s0, s38, 0
	v_lshl_add_u64 v[4:5], s[12:13], 0, v[4:5]
	v_add3_u32 v176, s0, v0, v3
	global_load_dword v0, v[4:5], off
	v_lshrrev_b32_e32 v124, 2, v1
	v_lshrrev_b32_e32 v125, 4, v1
	v_xor_b32_e32 v124, v124, v125
	v_and_b32_e32 v124, 1, v124
	v_add_u32_e32 v124, -1, v124
	v_and_b32_e32 v124, 0x38383838, v124
	v_mov_b32_e32 v200, 0
	v_mov_b32_e32 v201, 0
	v_mov_b32_e32 v202, 0
	v_mov_b32_e32 v203, 0
	v_mov_b32_e32 v204, 0
	v_mov_b32_e32 v125, v124
	v_mov_b32_e32 v126, v124
	v_mov_b32_e32 v127, v124
	v_mov_b32_e32 v128, v124
	v_mov_b32_e32 v129, v124
	v_mov_b32_e32 v130, v124
	v_mov_b32_e32 v131, v124
	v_mov_b32_e32 v140, 0x7f7f7f7f
	s_mov_b32 s0, 0xf800000
	s_movk_i32 s15, 0x3000
	s_mov_b32 s12, 1
	s_movk_i32 s14, 0x4000
	s_mov_b32 s13, 0x8000
	v_mov_b32_e32 v132, v141
	v_mov_b32_e32 v133, v141
	v_mov_b32_e32 v134, v141
	v_mov_b32_e32 v135, v141
	v_mov_b32_e32 v136, v141
	v_mov_b32_e32 v137, v141
	v_mov_b32_e32 v138, v141
	v_mov_b32_e32 v139, v141
	s_waitcnt vmcnt(5)
	v_mov_b32_e32 v4, v2
	v_mov_b32_e32 v5, v2
	v_mov_b32_e32 v6, v2
	v_mov_b32_e32 v7, v2
	v_mov_b32_e32 v8, v2
	v_mov_b32_e32 v9, v2
	v_mov_b32_e32 v10, v2
	v_mov_b32_e32 v11, v2
	v_mov_b32_e32 v12, v2
	v_mov_b32_e32 v13, v2
	v_mov_b32_e32 v14, v2
	v_mov_b32_e32 v15, v2
	v_mov_b32_e32 v16, v2
	v_mov_b32_e32 v17, v2
	v_mov_b32_e32 v3, v2
	v_mov_b64_e32 v[18:19], v[16:17]
	v_mov_b64_e32 v[16:17], v[14:15]
	v_mov_b64_e32 v[14:15], v[12:13]
	v_mov_b64_e32 v[12:13], v[10:11]
	v_mov_b64_e32 v[10:11], v[8:9]
	v_mov_b64_e32 v[8:9], v[6:7]
	v_mov_b64_e32 v[6:7], v[4:5]
	v_mov_b64_e32 v[4:5], v[2:3]
	s_waitcnt vmcnt(0) lgkmcnt(0)
	s_barrier
	ds_read_b128 v[24:27], v176 offset:1024
	ds_read_b128 v[20:23], v176
	ds_read_b128 v[36:39], v176 offset:512
	ds_read_b128 v[40:43], v176 offset:1536
	ds_read_b128 v[84:87], v176 offset:16384
	ds_read_b128 v[92:95], v176 offset:16896
	ds_read_b128 v[88:91], v176 offset:17408
	ds_read_b128 v[96:99], v176 offset:17920
	s_waitcnt vmcnt(3) lgkmcnt(6)
	v_mfma_f32_32x32x64_f8f6f4 v[20:35], v[20:27], v[116:123], v[4:19]
	v_mbcnt_lo_u32_b32 v3, -1, 0
	v_mbcnt_hi_u32_b32 v46, -1, v3
	v_and_b32_e32 v3, 64, v46
	v_xor_b32_e32 v47, 32, v46
	v_add_u32_e32 v48, 64, v3
	s_waitcnt vmcnt(2)
	v_max_f32_e32 v3, v44, v44
	s_waitcnt vmcnt(1)
	v_max_f32_e32 v44, v45, v45
	v_max_f32_e32 v44, v44, v3
	v_cmp_lt_i32_e32 vcc, v47, v48
	s_waitcnt vmcnt(0) lgkmcnt(0)
	s_barrier
	s_mov_b32 m0, s33
	s_nop 0
	buffer_load_dwordx4 v174, s[20:23], s15 offen lds
	s_add_i32 s15, s34, 0x4000
	s_mov_b32 m0, s15
	s_nop 0
	buffer_load_dwordx4 v174, s[24:27], s37 offen lds
	s_waitcnt lgkmcnt(4)
	v_mfma_f32_32x32x64_f8f6f4 v[4:19], v[36:43], v[116:123], v[4:19]
	s_nop 1
	v_max_f32_e32 v3, v21, v21
	v_max_f32_e32 v36, v20, v20
	v_max_f32_e32 v3, v36, v3
	v_xor_b32_e32 v38, 16, v46
	s_nop 13
	v_max3_f32 v37, v22, v23, v5
	v_max3_f32 v36, v37, v26, v27
	v_cndmask_b32_e32 v37, v46, v47, vcc
	v_lshlrev_b32_e32 v37, 2, v37
	ds_bpermute_b32 v37, v37, v44
	v_cmp_lt_i32_e32 vcc, v38, v48
	v_max3_f32 v3, v3, v4, v6
	v_max3_f32 v3, v3, v7, v24
	v_cndmask_b32_e32 v38, v46, v38, vcc
	s_waitcnt lgkmcnt(0)
	v_max_f32_e32 v37, v37, v37
	v_max_f32_e32 v37, v44, v37
	v_lshlrev_b32_e32 v38, 2, v38
	ds_bpermute_b32 v38, v38, v37
	v_max3_f32 v36, v36, v10, v11
	v_max3_f32 v3, v3, v25, v8
	v_max3_f32 v36, v36, v30, v31
	v_max3_f32 v3, v3, v9, v28
	s_waitcnt lgkmcnt(0)
	v_max_f32_e32 v38, v38, v38
	v_max_f32_e32 v37, v37, v38
	v_xor_b32_e32 v38, 8, v46
	v_cmp_lt_i32_e32 vcc, v38, v48
	v_max3_f32 v36, v36, v14, v15
	v_max3_f32 v3, v3, v29, v12
	v_cndmask_b32_e32 v38, v46, v38, vcc
	v_lshlrev_b32_e32 v38, 2, v38
	ds_bpermute_b32 v38, v38, v37
	v_max3_f32 v36, v36, v34, v35
	v_max3_f32 v3, v3, v13, v32
	v_max3_f32 v36, v36, v18, v19
	v_max3_f32 v3, v3, v33, v16
	s_waitcnt lgkmcnt(0)
	v_max_f32_e32 v38, v38, v38
	v_max_f32_e32 v37, v37, v38
	v_xor_b32_e32 v38, 4, v46
	v_cmp_lt_i32_e32 vcc, v38, v48
	v_max3_f32 v3, v3, v17, v36
	v_mov_b32_e32 v36, v3
	v_cndmask_b32_e32 v38, v46, v38, vcc
	v_lshlrev_b32_e32 v38, 2, v38
	ds_bpermute_b32 v38, v38, v37
	v_permlane32_swap_b32_e32 v3, v36
	v_max_f32_e32 v36, v36, v36
	v_max_f32_e32 v3, v3, v3
	s_waitcnt lgkmcnt(0)
	v_max_f32_e32 v38, v38, v38
	v_max_f32_e32 v37, v37, v38
	v_xor_b32_e32 v38, 2, v46
	v_cmp_lt_i32_e32 vcc, v38, v48
	v_max_f32_e32 v3, v3, v36
	v_sub_f32_e32 v36, 0xc0400000, v3
	v_cndmask_b32_e32 v38, v46, v38, vcc
	v_lshlrev_b32_e32 v38, 2, v38
	ds_bpermute_b32 v38, v38, v37
	v_add_f32_e32 v20, v36, v20
	v_add_f32_e32 v21, v36, v21
	v_add_f32_e32 v22, v36, v22
	v_add_f32_e32 v23, v36, v23
	s_waitcnt lgkmcnt(0)
	v_max_f32_e32 v38, v38, v38
	v_max_f32_e32 v37, v37, v38
	v_xor_b32_e32 v38, 1, v46
	v_cmp_lt_i32_e32 vcc, v38, v48
	v_add_f32_e32 v24, v36, v24
	v_add_f32_e32 v25, v36, v25
	v_cndmask_b32_e32 v38, v46, v38, vcc
	v_lshlrev_b32_e32 v38, 2, v38
	ds_bpermute_b32 v38, v38, v37
	v_add_f32_e32 v26, v36, v26
	v_add_f32_e32 v27, v36, v27
	v_add_f32_e32 v28, v36, v28
	v_add_f32_e32 v29, v36, v29
	s_waitcnt lgkmcnt(0)
	v_max_f32_e32 v38, v38, v38
	v_max_f32_e32 v37, v37, v38
	v_mul_f32_e32 v38, 0x4f800000, v37
	v_cmp_gt_f32_e32 vcc, s0, v37
	v_add_f32_e32 v30, v36, v30
	v_add_f32_e32 v31, v36, v31
	v_cndmask_b32_e32 v37, v37, v38, vcc
	v_sqrt_f32_e32 v38, v37
	v_add_f32_e32 v32, v36, v32
	v_add_f32_e32 v33, v36, v33
	v_add_f32_e32 v34, v36, v34
	v_add_f32_e32 v35, v36, v35
	v_add_f32_e32 v4, v36, v4
	v_add_f32_e32 v5, v36, v5
	v_add_f32_e32 v6, v36, v6
	v_add_f32_e32 v7, v36, v7
	v_add_f32_e32 v8, v36, v8
	v_add_f32_e32 v9, v36, v9
	v_add_f32_e32 v10, v36, v10
	v_add_f32_e32 v11, v36, v11
	v_add_f32_e32 v12, v36, v12
	v_add_f32_e32 v13, v36, v13
	v_add_f32_e32 v14, v36, v14
	v_add_f32_e32 v15, v36, v15
	v_add_f32_e32 v16, v36, v16
	v_add_f32_e32 v17, v36, v17
	v_add_f32_e32 v18, v36, v18
	v_add_f32_e32 v19, v36, v19
	v_add_u32_e32 v36, -1, v38
	v_fma_f32 v39, -v36, v38, v37
	v_cmp_ge_f32_e64 s[0:1], 0, v39
	v_add_u32_e32 v39, 1, v38
	v_exp_f32_e32 v161, v20
	v_cndmask_b32_e64 v36, v38, v36, s[0:1]
	v_fma_f32 v38, -v39, v38, v37
	v_cmp_lt_f32_e64 s[0:1], 0, v38
	v_exp_f32_e32 v100, v4
	v_exp_f32_e32 v163, v21
	v_cndmask_b32_e64 v36, v36, v39, s[0:1]
	v_mul_f32_e32 v38, 0x37800000, v36
	v_cndmask_b32_e32 v36, v36, v38, vcc
	v_mov_b32_e32 v38, 0x260
	v_cmp_class_f32_e32 vcc, v37, v38
	s_mov_b32 s0, 0x42700000
	v_exp_f32_e32 v148, v5
	v_cndmask_b32_e32 v36, v36, v37, vcc
	s_waitcnt vmcnt(0)
	v_mul_f32_e32 v0, v36, v0
	v_mul_f32_e32 v0, 0x3f91eb85, v0
	v_exp_f32_e32 v162, v22
	v_exp_f32_e32 v101, v6
	v_exp_f32_e32 v164, v23
	v_exp_f32_e32 v102, v7
	v_exp_f32_e32 v150, v24
	v_exp_f32_e32 v143, v8
	v_exp_f32_e32 v154, v25
	v_exp_f32_e32 v146, v9
	v_exp_f32_e32 v152, v26
	v_exp_f32_e32 v145, v10
	v_exp_f32_e32 v157, v27
	v_exp_f32_e32 v147, v11
	v_exp_f32_e32 v149, v28
	v_exp_f32_e32 v69, v12
	v_exp_f32_e32 v153, v29
	v_exp_f32_e32 v109, v13
	v_exp_f32_e32 v151, v30
	v_exp_f32_e32 v108, v14
	v_exp_f32_e32 v156, v31
	v_exp_f32_e32 v142, v15
	v_exp_f32_e32 v155, v32
	v_exp_f32_e32 v110, v16
	v_exp_f32_e32 v159, v33
	v_exp_f32_e32 v144, v17
	v_exp_f32_e32 v158, v34
	v_exp_f32_e32 v111, v18
	v_exp_f32_e32 v160, v35
	v_exp_f32_e32 v114, v19
	v_cmp_nge_f32_e64 s[0:1], s0, v0
	v_sub_f32_e32 v0, v2, v3
	v_add_f32_e32 v36, 0xc0400000, v0
	v_mov_b32_e32 v37, v36
	v_mov_b32_e32 v38, v36
	v_mov_b32_e32 v39, v36
	v_mov_b32_e32 v40, v36
	v_mov_b32_e32 v41, v36
	v_mov_b32_e32 v42, v36
	v_mov_b32_e32 v43, v36
	v_mov_b32_e32 v44, v36
	v_mov_b32_e32 v45, v36
	v_mov_b32_e32 v46, v36
	v_mov_b32_e32 v47, v36
	v_mov_b32_e32 v48, v36
	v_mov_b32_e32 v49, v36
	v_mov_b32_e32 v50, v36
	v_mov_b32_e32 v51, v36
	v_mov_b32_e32 v4, v141
	v_mov_b32_e32 v5, v141
	v_mov_b32_e32 v6, v141
	v_mov_b32_e32 v7, v141
	v_mov_b32_e32 v8, v141
	v_mov_b32_e32 v9, v141
	v_mov_b32_e32 v10, v141
	v_mov_b32_e32 v11, v141
	v_mov_b32_e32 v12, v141
	v_mov_b32_e32 v13, v141
	v_mov_b32_e32 v14, v141
	v_mov_b32_e32 v15, v141
	v_mov_b32_e32 v16, v141
	v_mov_b32_e32 v17, v141
	v_mov_b32_e32 v18, v141
	v_mov_b32_e32 v19, v141
	v_mov_b32_e32 v20, v141
	v_mov_b32_e32 v21, v141
	v_mov_b32_e32 v22, v141
	v_mov_b32_e32 v23, v141
	v_mov_b32_e32 v24, v141
	v_mov_b32_e32 v25, v141
	v_mov_b32_e32 v26, v141
	v_mov_b32_e32 v27, v141
	v_mov_b32_e32 v28, v141
	v_mov_b32_e32 v29, v141
	v_mov_b32_e32 v30, v141
	v_mov_b32_e32 v31, v141
	v_mov_b32_e32 v32, v141
	v_mov_b32_e32 v33, v141
	v_mov_b32_e32 v34, v141
	v_mov_b32_e32 v35, v141
	v_mov_b32_e32 v0, v141
.LBB1_1:
	v_mfma_f32_32x32x64_f8f6f4 v[76:91], v[84:91], v[116:123], v[36:51]
	v_cvt_pk_fp8_f32 v132, v161, v163
	v_add_u32_e32 v68, s36, v176
	v_cvt_pk_fp8_f32 v132, v162, v164 op_sel:[0,0,1]
	ds_read_b128 v[162:165], v68 offset:49152
	ds_read_b128 v[166:169], v68 offset:50176
	v_cvt_pk_fp8_f32 v133, v150, v154
	v_cvt_pk_fp8_f32 v133, v152, v157 op_sel:[0,0,1]
	s_lshl_b32 s16, s12, 12
	s_add_i32 s15, s16, 0x3000
	s_add_i32 s17, s14, s33
	s_mov_b32 m0, s17
	s_nop 0
	buffer_load_dwordx4 v174, s[20:23], s15 offen lds
	v_cvt_pk_fp8_f32 v134, v149, v153
	v_cvt_pk_fp8_f32 v134, v151, v156 op_sel:[0,0,1]
	v_cvt_pk_fp8_f32 v135, v155, v159
	v_cvt_pk_fp8_f32 v135, v158, v160 op_sel:[0,0,1]
	v_cvt_pk_fp8_f32 v136, v100, v148
	v_cvt_pk_fp8_f32 v136, v101, v102 op_sel:[0,0,1]
	s_waitcnt lgkmcnt(2)
	v_mfma_f32_32x32x64_f8f6f4 v[92:107], v[92:99], v[116:123], v[36:51]
	ds_read_b128 v[148:151], v68 offset:49664
	ds_read_b128 v[152:155], v68 offset:50688
	v_cvt_pk_fp8_f32 v137, v143, v146
	v_cvt_pk_fp8_f32 v137, v145, v147 op_sel:[0,0,1]
	s_add_i32 s15, s16, 0x1000
	s_add_i32 s17, s13, s34
	s_mov_b32 m0, s17
	s_nop 0
	buffer_load_dwordx4 v174, s[24:27], s15 offen lds
	v_cvt_pk_fp8_f32 v138, v69, v109
	v_cvt_pk_fp8_f32 v138, v108, v142 op_sel:[0,0,1]
	v_cvt_pk_fp8_f32 v139, v110, v144
	v_cvt_pk_fp8_f32 v139, v111, v114 op_sel:[0,0,1]
	s_waitcnt lgkmcnt(2)
	s_nop 0
	v_mfma_f32_32x32x64_f8f6f4 v[4:19], v[162:169], v[132:139], v[4:19]
	v_exp_f32_e32 v142, v76
	v_exp_f32_e32 v143, v77
	v_exp_f32_e32 v144, v78
	v_exp_f32_e32 v145, v79
	v_exp_f32_e32 v146, v80
	v_exp_f32_e32 v147, v81
	v_exp_f32_e32 v156, v82
	v_exp_f32_e32 v157, v83
	v_add_u32_e32 v158, s13, v176
	ds_read_b128 v[108:111], v158
	ds_read_b128 v[112:115], v158 offset:1024
	ds_read_b128 v[52:55], v158 offset:512
	ds_read_b128 v[56:59], v158 offset:1536
	v_exp_f32_e32 v159, v84
	v_exp_f32_e32 v160, v85
	v_mfma_f32_16x16x128_f8f6f4 v[200:203], v[124:131], v[132:139], v[200:203]
	v_exp_f32_e32 v161, v86
	v_exp_f32_e32 v162, v87
	v_exp_f32_e32 v163, v88
	v_exp_f32_e32 v164, v89
	v_exp_f32_e32 v165, v90
	v_exp_f32_e32 v166, v91
	s_waitcnt lgkmcnt(4)
	v_mfma_f32_32x32x64_f8f6f4 v[20:35], v[148:155], v[132:139], v[20:35]
	v_exp_f32_e32 v167, v92
	v_exp_f32_e32 v168, v93
	v_exp_f32_e32 v169, v94
	v_exp_f32_e32 v170, v95
	v_exp_f32_e32 v148, v96
	v_exp_f32_e32 v149, v97
	v_exp_f32_e32 v150, v98
	v_exp_f32_e32 v151, v99
	v_exp_f32_e32 v152, v100
	v_exp_f32_e32 v153, v101
	v_exp_f32_e32 v154, v102
	v_exp_f32_e32 v155, v103
	v_exp_f32_e32 v158, v104
	v_exp_f32_e32 v171, v105
	v_exp_f32_e32 v177, v106
	v_exp_f32_e32 v186, v107
	s_add_i32 s15, s13, 0x4000
	s_cmpk_lg_u32 s13, 0x8000
	s_cselect_b32 s15, s15, 0
	s_waitcnt vmcnt(2) lgkmcnt(0)
	s_barrier
	v_mfma_f32_32x32x64_f8f6f4 v[84:99], v[108:115], v[116:123], v[36:51]
	v_cvt_pk_fp8_f32 v132, v142, v143
	v_add_u32_e32 v142, s14, v176
	v_cvt_pk_fp8_f32 v132, v144, v145 op_sel:[0,0,1]
	ds_read_b128 v[60:63], v142 offset:49152
	ds_read_b128 v[64:67], v142 offset:50176
	v_cvt_pk_fp8_f32 v133, v146, v147
	v_cvt_pk_fp8_f32 v133, v156, v157 op_sel:[0,0,1]
	s_add_i32 s14, s16, 0x4000
	s_add_i32 s17, s13, s33
	s_mov_b32 m0, s17
	s_nop 0
	buffer_load_dwordx4 v174, s[20:23], s14 offen lds
	v_cvt_pk_fp8_f32 v134, v159, v160
	v_cvt_pk_fp8_f32 v134, v161, v162 op_sel:[0,0,1]
	v_cvt_pk_fp8_f32 v135, v163, v164
	v_cvt_pk_fp8_f32 v135, v165, v166 op_sel:[0,0,1]
	s_waitcnt lgkmcnt(2)
	v_mfma_f32_32x32x64_f8f6f4 v[100:115], v[52:59], v[116:123], v[36:51]
	v_cvt_pk_fp8_f32 v136, v167, v168
	v_cvt_pk_fp8_f32 v136, v169, v170 op_sel:[0,0,1]
	ds_read_b128 v[178:181], v142 offset:49664
	ds_read_b128 v[182:185], v142 offset:50688
	v_cvt_pk_fp8_f32 v137, v148, v149
	v_cvt_pk_fp8_f32 v137, v150, v151 op_sel:[0,0,1]
	s_addk_i32 s16, 0x2000
	s_add_i32 s14, s15, s34
	s_mov_b32 m0, s14
	s_nop 0
	buffer_load_dwordx4 v174, s[24:27], s16 offen lds
	v_cvt_pk_fp8_f32 v138, v152, v153
	v_cvt_pk_fp8_f32 v138, v154, v155 op_sel:[0,0,1]
	v_cvt_pk_fp8_f32 v139, v158, v171
	v_cvt_pk_fp8_f32 v139, v177, v186 op_sel:[0,0,1]
	v_sub_f32_e32 v52, v200, v204
	v_mov_b32_e32 v204, v200
	v_max_f32_e32 v0, v0, v0
	v_max_f32_e32 v0, v0, v52
	s_waitcnt lgkmcnt(2)
	v_mfma_f32_32x32x64_f8f6f4 v[4:19], v[60:67], v[132:139], v[4:19]
	v_exp_f32_e32 v161, v84
	v_exp_f32_e32 v163, v85
	v_exp_f32_e32 v162, v86
	v_exp_f32_e32 v164, v87
	v_exp_f32_e32 v150, v88
	v_exp_f32_e32 v154, v89
	v_exp_f32_e32 v152, v90
	v_exp_f32_e32 v157, v91
	v_add_u32_e32 v141, s15, v176
	ds_read_b128 v[84:87], v141
	ds_read_b128 v[88:91], v141 offset:1024
	v_mfma_f32_16x16x128_f8f6f4 v[200:203], v[124:131], v[132:139], v[200:203]
	v_exp_f32_e32 v149, v92
	v_exp_f32_e32 v153, v93
	v_exp_f32_e32 v151, v94
	v_exp_f32_e32 v156, v95
	v_exp_f32_e32 v155, v96
	v_exp_f32_e32 v159, v97
	v_exp_f32_e32 v158, v98
	v_exp_f32_e32 v160, v99
	ds_read_b128 v[92:95], v141 offset:512
	ds_read_b128 v[96:99], v141 offset:1536
	s_waitcnt lgkmcnt(4)
	v_mfma_f32_32x32x64_f8f6f4 v[20:35], v[178:185], v[132:139], v[20:35]
	v_exp_f32_e32 v100, v100
	v_exp_f32_e32 v148, v101
	v_exp_f32_e32 v101, v102
	v_exp_f32_e32 v102, v103
	v_exp_f32_e32 v143, v104
	v_exp_f32_e32 v146, v105
	v_exp_f32_e32 v145, v106
	v_exp_f32_e32 v147, v107
	v_exp_f32_e32 v69, v108
	v_exp_f32_e32 v109, v109
	v_exp_f32_e32 v108, v110
	v_exp_f32_e32 v142, v111
	v_exp_f32_e32 v110, v112
	v_exp_f32_e32 v144, v113
	v_exp_f32_e32 v111, v114
	v_exp_f32_e32 v114, v115
	s_add_i32 s16, s15, 0x4000
	s_cmpk_lg_u32 s15, 0x8000
	s_mov_b32 s36, s13
	s_mov_b32 s14, s15
	s_cselect_b32 s13, s16, 0
	s_add_i32 s12, s12, 2
	s_cmp_gt_u32 s12, 26
	s_waitcnt vmcnt(2) lgkmcnt(0)
	s_barrier
	s_cbranch_scc0 .LBB1_1
	s_and_b32 s41, s2, 3
	s_lshl_b32 s42, s41, 6
	s_lshl_b32 s43, s3, 5
	s_add_i32 s42, s42, s43
	v_add_u32_e32 v198, s42, v172
	v_lshlrev_b32_e32 v198, 8, v198
	v_lshl_add_u32 v198, v175, 4, v198
	s_lshl_b32 s44, s41, 8
	s_lshl_b32 s45, s3, 7
	s_add_i32 s44, s44, s45
	v_lshl_add_u32 v199, v175, 4, s44
	s_lshl_b32 s46, s41, 2
	v_mov_b32_e32 v205, s46
	v_add_u32_e32 v113, 0xc000, v176
	v_mov_b32_e32 v112, 0x7f7f7f7f
	v_cvt_pk_fp8_f32 v132, v161, v163
	v_cvt_pk_fp8_f32 v132, v162, v164 op_sel:[0,0,1]
	s_waitcnt lgkmcnt(2)
	v_mfma_f32_32x32x64_f8f6f4 v[70:85], v[84:91], v[116:123], v[36:51]
	ds_read_b128 v[162:165], v113 offset:32768
	ds_read_b128 v[166:169], v113 offset:33792
	v_cvt_pk_fp8_f32 v133, v150, v154
	v_cvt_pk_fp8_f32 v133, v152, v157 op_sel:[0,0,1]
	s_mov_b32 s13, 0x1e000
	s_mov_b32 m0, s33
	s_nop 0
	buffer_load_dwordx4 v174, s[20:23], s13 offen lds
	v_cvt_pk_fp8_f32 v134, v149, v153
	v_cvt_pk_fp8_f32 v134, v151, v156 op_sel:[0,0,1]
	v_cvt_pk_fp8_f32 v135, v155, v159
	v_cvt_pk_fp8_f32 v135, v158, v160 op_sel:[0,0,1]
	v_cvt_pk_fp8_f32 v136, v100, v148
	v_cvt_pk_fp8_f32 v136, v101, v102 op_sel:[0,0,1]
	s_waitcnt lgkmcnt(2)
	v_mfma_f32_32x32x64_f8f6f4 v[86:101], v[92:99], v[116:123], v[36:51]
	ds_read_b128 v[148:151], v113 offset:33280
	ds_read_b128 v[152:155], v113 offset:34304
	v_cvt_pk_fp8_f32 v137, v143, v146
	v_cvt_pk_fp8_f32 v137, v145, v147 op_sel:[0,0,1]
	s_cmp_lg_u32 0, -1
	s_cselect_b32 s12, 0, 0
	s_add_i32 s15, s12, s35
	s_add_i32 s12, s15, 0x10000
	s_mov_b32 s26, s22
	s_mov_b32 s27, s23
	s_mov_b32 s14, 0x1c000
	s_mov_b32 m0, s12
	s_nop 0
	buffer_load_dwordx4 v174, s[24:27], s14 offen lds
	global_load_dwordx4 v[208:211], v198, s[4:5]
	global_load_dwordx4 v[212:215], v198, s[4:5] offset:32
	global_load_dwordx4 v[216:219], v198, s[4:5] offset:64
	global_load_dwordx4 v[220:223], v198, s[4:5] offset:96
	global_load_dwordx4 v[224:227], v198, s[4:5] offset:128
	v_cvt_pk_fp8_f32 v138, v69, v109
	v_cvt_pk_fp8_f32 v138, v108, v142 op_sel:[0,0,1]
	v_cvt_pk_fp8_f32 v139, v110, v144
	v_cvt_pk_fp8_f32 v139, v111, v114 op_sel:[0,0,1]
	s_waitcnt lgkmcnt(2)
	s_nop 0
	v_mfma_f32_32x32x64_f8f6f4 v[4:19], v[162:169], v[132:139], v[4:19]
	v_exp_f32_e32 v104, v73
	v_exp_f32_e32 v69, v70
	v_exp_f32_e32 v102, v71
	v_exp_f32_e32 v103, v72
	v_exp_f32_e32 v110, v74
	v_exp_f32_e32 v111, v75
	v_exp_f32_e32 v114, v76
	v_exp_f32_e32 v115, v77
	ds_read_b128 v[70:73], v176 offset:16384
	ds_read_b128 v[74:77], v176 offset:17408
	v_mfma_f32_16x16x128_f8f6f4 v[200:203], v[124:131], v[132:139], v[200:203]
	v_exp_f32_e32 v140, v78
	v_exp_f32_e32 v141, v79
	v_exp_f32_e32 v142, v80
	v_exp_f32_e32 v143, v81
	v_exp_f32_e32 v144, v82
	v_exp_f32_e32 v145, v83
	v_exp_f32_e32 v146, v84
	v_exp_f32_e32 v147, v85
	s_waitcnt lgkmcnt(2)
	v_mfma_f32_32x32x64_f8f6f4 v[20:35], v[148:155], v[132:139], v[20:35]
	v_exp_f32_e32 v156, v86
	v_exp_f32_e32 v157, v87
	v_exp_f32_e32 v158, v88
	v_exp_f32_e32 v159, v89
	v_exp_f32_e32 v148, v90
	v_exp_f32_e32 v149, v91
	v_exp_f32_e32 v150, v92
	v_exp_f32_e32 v151, v93
	ds_read_b128 v[86:89], v176 offset:16896
	ds_read_b128 v[90:93], v176 offset:17920
	v_exp_f32_e32 v152, v94
	v_exp_f32_e32 v153, v95
	v_exp_f32_e32 v154, v96
	v_exp_f32_e32 v155, v97
	v_exp_f32_e32 v160, v98
	v_exp_f32_e32 v161, v99
	v_exp_f32_e32 v162, v100
	v_exp_f32_e32 v163, v101
	s_waitcnt vmcnt(7) lgkmcnt(0)
	s_barrier
	s_waitcnt lgkmcnt(2)
	v_mfma_f32_32x32x64_f8f6f4 v[70:85], v[70:77], v[116:123], v[36:51]
	v_cvt_pk_fp8_f32 v132, v69, v102
	v_cvt_pk_fp8_f32 v132, v103, v104 op_sel:[0,0,1]
	ds_read_b128 v[102:105], v176 offset:49152
	ds_read_b128 v[106:109], v176 offset:50176
	v_cvt_pk_fp8_f32 v133, v110, v111
	v_cvt_pk_fp8_f32 v133, v114, v115 op_sel:[0,0,1]
	s_add_i32 s16, s15, 0x4000
	s_mov_b32 s14, 0x1f000
	s_mov_b32 m0, s16
	s_nop 0
	buffer_load_dwordx4 v174, s[20:23], s14 offen lds
	v_cvt_pk_fp8_f32 v134, v140, v141
	v_cvt_pk_fp8_f32 v134, v142, v143 op_sel:[0,0,1]
	v_cvt_pk_fp8_f32 v135, v144, v145
	v_cvt_pk_fp8_f32 v135, v146, v147 op_sel:[0,0,1]
	s_waitcnt lgkmcnt(2)
	v_mfma_f32_32x32x64_f8f6f4 v[86:101], v[86:93], v[116:123], v[36:51]
	v_cvt_pk_fp8_f32 v136, v156, v157
	v_cvt_pk_fp8_f32 v136, v158, v159 op_sel:[0,0,1]
	ds_read_b128 v[140:143], v176 offset:49664
	ds_read_b128 v[144:147], v176 offset:50688
	v_cvt_pk_fp8_f32 v137, v148, v149
	v_cvt_pk_fp8_f32 v137, v150, v151 op_sel:[0,0,1]
	s_add_i32 s15, s15, 0x14000
	s_mov_b32 s16, 0x1d000
	s_mov_b32 m0, s15
	s_nop 0
	buffer_load_dwordx4 v174, s[24:27], s16 offen lds
	global_load_dwordx4 v[228:231], v198, s[4:5] offset:160
	global_load_dwordx4 v[232:235], v198, s[4:5] offset:192
	global_load_dwordx4 v[236:239], v198, s[4:5] offset:224
	global_load_dwordx4 v[240:243], v199, s[6:7]
	v_cvt_pk_fp8_f32 v138, v152, v153
	v_cvt_pk_fp8_f32 v138, v154, v155 op_sel:[0,0,1]
	v_cvt_pk_fp8_f32 v139, v160, v161
	v_cvt_pk_fp8_f32 v139, v162, v163 op_sel:[0,0,1]
	v_sub_f32_e32 v114, v200, v204
	v_mov_b32_e32 v204, v200
	s_waitcnt lgkmcnt(2)
	v_mfma_f32_32x32x64_f8f6f4 v[4:19], v[102:109], v[132:139], v[4:19]
	v_exp_f32_e32 v110, v70
	v_exp_f32_e32 v111, v71
	v_exp_f32_e32 v148, v73
	v_exp_f32_e32 v115, v72
	v_exp_f32_e32 v149, v74
	v_exp_f32_e32 v150, v75
	v_exp_f32_e32 v151, v76
	v_exp_f32_e32 v152, v77
	ds_read_b128 v[70:73], v176 offset:32768
	ds_read_b128 v[74:77], v176 offset:33792
	v_mfma_f32_16x16x128_f8f6f4 v[200:203], v[124:131], v[132:139], v[200:203]
	v_exp_f32_e32 v153, v78
	v_exp_f32_e32 v154, v79
	v_exp_f32_e32 v155, v80
	v_exp_f32_e32 v156, v81
	v_exp_f32_e32 v157, v83
	v_exp_f32_e32 v158, v84
	v_exp_f32_e32 v159, v85
	s_nop 7
	v_exp_f32_e32 v53, v82
	s_waitcnt lgkmcnt(2)
	v_mfma_f32_32x32x64_f8f6f4 v[20:35], v[140:147], v[132:139], v[20:35]
	v_exp_f32_e32 v160, v86
	v_exp_f32_e32 v161, v87
	v_exp_f32_e32 v162, v88
	v_exp_f32_e32 v163, v89
	v_exp_f32_e32 v164, v90
	v_exp_f32_e32 v165, v91
	v_exp_f32_e32 v166, v92
	v_exp_f32_e32 v167, v93
	ds_read_b128 v[78:81], v176 offset:33280
	ds_read_b128 v[82:85], v176 offset:34304
	v_exp_f32_e32 v168, v94
	v_exp_f32_e32 v169, v95
	v_exp_f32_e32 v170, v96
	v_exp_f32_e32 v171, v97
	v_exp_f32_e32 v177, v98
	v_exp_f32_e32 v178, v99
	v_exp_f32_e32 v179, v100
	v_exp_f32_e32 v180, v101
	s_waitcnt vmcnt(11) lgkmcnt(0)
	s_barrier
	s_waitcnt lgkmcnt(2)
	v_mfma_f32_32x32x64_f8f6f4 v[86:101], v[70:77], v[116:123], v[36:51]
	v_cvt_pk_fp8_f32 v132, v110, v111
	v_cvt_pk_fp8_f32 v132, v115, v148 op_sel:[0,0,1]
	ds_read_b128 v[102:105], v113 offset:16384
	ds_read_b128 v[106:109], v113 offset:17408
	v_cvt_pk_fp8_f32 v133, v149, v150
	v_cvt_pk_fp8_f32 v133, v151, v152 op_sel:[0,0,1]
	v_cvt_pk_fp8_f32 v134, v153, v154
	v_cvt_pk_fp8_f32 v134, v155, v156 op_sel:[0,0,1]
	v_cvt_pk_fp8_f32 v135, v53, v157
	v_cvt_pk_fp8_f32 v135, v158, v159 op_sel:[0,0,1]
	s_waitcnt lgkmcnt(2)
	v_mfma_f32_32x32x64_f8f6f4 v[70:85], v[78:85], v[116:123], v[36:51]
	v_cvt_pk_fp8_f32 v136, v160, v161
	v_cvt_pk_fp8_f32 v136, v162, v163 op_sel:[0,0,1]
	ds_read_b128 v[140:143], v113 offset:16896
	ds_read_b128 v[144:147], v113 offset:17920
	v_cvt_pk_fp8_f32 v137, v164, v165
	v_cvt_pk_fp8_f32 v137, v166, v167 op_sel:[0,0,1]
	s_mov_b32 m0, s34
	s_nop 0
	buffer_load_dwordx4 v174, s[24:27], s13 offen lds
	global_load_dwordx4 v[244:247], v199, s[6:7] offset:32
	global_load_dwordx4 v[248:251], v199, s[6:7] offset:64
	global_load_dwordx4 v[252:255], v199, s[6:7] offset:96
	global_load_dword v205, v205, s[8:9]
	v_cvt_pk_fp8_f32 v138, v168, v169
	v_cvt_pk_fp8_f32 v138, v170, v171 op_sel:[0,0,1]
	v_cvt_pk_fp8_f32 v139, v177, v178
	v_cvt_pk_fp8_f32 v139, v179, v180 op_sel:[0,0,1]
	s_waitcnt lgkmcnt(2)
	s_nop 0
	v_mfma_f32_32x32x64_f8f6f4 v[4:19], v[102:109], v[132:139], v[4:19]
	v_exp_f32_e32 v148, v88
	v_exp_f32_e32 v149, v89
	v_exp_f32_e32 v53, v86
	v_exp_f32_e32 v115, v87
	v_exp_f32_e32 v150, v92
	v_exp_f32_e32 v151, v93
	v_exp_f32_e32 v102, v90
	v_exp_f32_e32 v103, v91
	ds_read_b128 v[86:89], v176
	ds_read_b128 v[90:93], v176 offset:1024
	v_mfma_f32_16x16x128_f8f6f4 v[200:203], v[124:131], v[132:139], v[200:203]
	v_exp_f32_e32 v152, v94
	v_exp_f32_e32 v153, v95
	v_exp_f32_e32 v154, v96
	v_exp_f32_e32 v155, v97
	v_exp_f32_e32 v156, v98
	v_exp_f32_e32 v157, v99
	v_exp_f32_e32 v158, v100
	v_exp_f32_e32 v159, v101
	s_waitcnt lgkmcnt(2)
	v_mfma_f32_32x32x64_f8f6f4 v[20:35], v[140:147], v[132:139], v[20:35]
	v_exp_f32_e32 v160, v70
	v_exp_f32_e32 v161, v71
	v_exp_f32_e32 v162, v72
	v_exp_f32_e32 v163, v73
	v_exp_f32_e32 v164, v74
	v_exp_f32_e32 v165, v75
	v_exp_f32_e32 v166, v76
	v_exp_f32_e32 v167, v77
	ds_read_b128 v[94:97], v176 offset:512
	ds_read_b128 v[98:101], v176 offset:1536
	v_exp_f32_e32 v168, v78
	v_exp_f32_e32 v169, v79
	v_exp_f32_e32 v170, v80
	v_exp_f32_e32 v171, v81
	v_exp_f32_e32 v177, v82
	v_exp_f32_e32 v178, v83
	v_exp_f32_e32 v179, v84
	v_exp_f32_e32 v180, v85
	s_waitcnt vmcnt(9) lgkmcnt(0)
	s_barrier
	s_waitcnt lgkmcnt(2)
	v_mfma_f32_32x32x64_f8f6f4 v[70:85], v[86:93], v[116:123], v[36:51]
	ds_read_b128 v[104:107], v113 offset:32768
	ds_read_b128 v[108:111], v113 offset:33792
	v_cvt_pk_fp8_f32 v132, v53, v115
	v_cvt_pk_fp8_f32 v133, v102, v103
	v_cvt_pk_fp8_f32 v134, v152, v153
	v_cvt_pk_fp8_f32 v132, v148, v149 op_sel:[0,0,1]
	v_cvt_pk_fp8_f32 v133, v150, v151 op_sel:[0,0,1]
	v_cvt_pk_fp8_f32 v134, v154, v155 op_sel:[0,0,1]
	v_cvt_pk_fp8_f32 v135, v156, v157
	v_cvt_pk_fp8_f32 v135, v158, v159 op_sel:[0,0,1]
	s_waitcnt lgkmcnt(2)
	v_mfma_f32_32x32x64_f8f6f4 v[86:101], v[94:101], v[116:123], v[36:51]
	v_cvt_pk_fp8_f32 v136, v160, v161
	v_cvt_pk_fp8_f32 v136, v162, v163 op_sel:[0,0,1]
	ds_read_b128 v[140:143], v113 offset:33280
	ds_read_b128 v[144:147], v113 offset:34304
	v_cvt_pk_fp8_f32 v137, v164, v165
	v_cvt_pk_fp8_f32 v137, v166, v167 op_sel:[0,0,1]
	s_mov_b32 m0, s12
	s_nop 0
	buffer_load_dwordx4 v174, s[24:27], s14 offen lds
	v_cvt_pk_fp8_f32 v138, v168, v169
	v_cvt_pk_fp8_f32 v138, v170, v171 op_sel:[0,0,1]
	v_cvt_pk_fp8_f32 v139, v177, v178
	v_cvt_pk_fp8_f32 v139, v179, v180 op_sel:[0,0,1]
	v_sub_f32_e32 v52, v200, v204
	v_mov_b32_e32 v204, v200
	v_max3_f32 v0, v0, v114, v52
	v_exp_f32_e32 v72, v72
	v_exp_f32_e32 v73, v73
	v_exp_f32_e32 v52, v70
	v_exp_f32_e32 v53, v71
	v_exp_f32_e32 v102, v74
	v_exp_f32_e32 v103, v75
	v_exp_f32_e32 v114, v76
	v_exp_f32_e32 v115, v77
	ds_read_b128 v[150:153], v176 offset:16384
	ds_read_b128 v[154:157], v176 offset:17408
	v_mfma_f32_16x16x128_f8f6f4 v[200:203], v[124:131], v[132:139], v[200:203]
	v_exp_f32_e32 v177, v78
	v_exp_f32_e32 v178, v79
	v_exp_f32_e32 v179, v80
	v_exp_f32_e32 v180, v81
	s_nop 10
	v_exp_f32_e32 v55, v82
	v_exp_f32_e32 v181, v83
	v_exp_f32_e32 v182, v84
	v_exp_f32_e32 v183, v85
	v_exp_f32_e32 v184, v86
	v_exp_f32_e32 v185, v87
	v_exp_f32_e32 v88, v88
	v_exp_f32_e32 v89, v89
	v_exp_f32_e32 v186, v90
	v_exp_f32_e32 v187, v91
	v_exp_f32_e32 v188, v92
	v_exp_f32_e32 v189, v93
	ds_read_b128 v[164:167], v176 offset:16896
	ds_read_b128 v[168:171], v176 offset:17920
	v_exp_f32_e32 v190, v94
	v_exp_f32_e32 v191, v95
	v_exp_f32_e32 v192, v96
	v_exp_f32_e32 v193, v97
	v_exp_f32_e32 v194, v98
	v_exp_f32_e32 v195, v99
	v_exp_f32_e32 v196, v100
	v_exp_f32_e32 v197, v101
	s_waitcnt vmcnt(0) lgkmcnt(0)
	s_barrier
	v_mov_b32_e32 v148, v132
	v_cvt_pk_fp8_f32 v148, v52, v53
	v_cvt_pk_fp8_f32 v148, v72, v73 op_sel:[0,0,1]
	s_waitcnt lgkmcnt(2)
	v_mfma_f32_32x32x64_f8f6f4 v[72:87], v[150:157], v[116:123], v[36:51]
	ds_read_b128 v[156:159], v176 offset:49152
	ds_read_b128 v[160:163], v176 offset:50176
	v_mov_b32_e32 v149, v133
	v_cvt_pk_fp8_f32 v149, v102, v103
	v_cvt_pk_fp8_f32 v149, v114, v115 op_sel:[0,0,1]
	v_mov_b32_e32 v150, v134
	v_cvt_pk_fp8_f32 v150, v177, v178
	v_cvt_pk_fp8_f32 v150, v179, v180 op_sel:[0,0,1]
	v_mov_b32_e32 v151, v135
	v_cvt_pk_fp8_f32 v151, v55, v181
	v_cvt_pk_fp8_f32 v151, v182, v183 op_sel:[0,0,1]
	v_mov_b32_e32 v152, v136
	v_cvt_pk_fp8_f32 v152, v184, v185
	v_cvt_pk_fp8_f32 v152, v88, v89 op_sel:[0,0,1]
	s_waitcnt lgkmcnt(2)
	v_mfma_f32_32x32x64_f8f6f4 v[88:103], v[164:171], v[116:123], v[36:51]
	ds_read_b128 v[164:167], v176 offset:49664
	ds_read_b128 v[168:171], v176 offset:50688
	v_mov_b32_e32 v153, v137
	v_cvt_pk_fp8_f32 v153, v186, v187
	v_cvt_pk_fp8_f32 v153, v188, v189 op_sel:[0,0,1]
	v_mov_b32_e32 v154, v138
	v_cvt_pk_fp8_f32 v154, v190, v191
	v_cvt_pk_fp8_f32 v154, v192, v193 op_sel:[0,0,1]
	v_mov_b32_e32 v155, v139
	v_cvt_pk_fp8_f32 v155, v194, v195
	v_cvt_pk_fp8_f32 v155, v196, v197 op_sel:[0,0,1]
	v_sub_f32_e32 v52, v200, v204
	v_mov_b32_e32 v204, v200
	s_nop 2
	v_exp_f32_e32 v36, v72
	v_exp_f32_e32 v37, v73
	v_exp_f32_e32 v38, v74
	v_exp_f32_e32 v39, v75
	v_exp_f32_e32 v40, v76
	v_exp_f32_e32 v41, v77
	v_exp_f32_e32 v42, v78
	v_exp_f32_e32 v43, v79
	v_exp_f32_e32 v53, v80
	v_exp_f32_e32 v80, v83
	v_exp_f32_e32 v54, v81
	v_exp_f32_e32 v55, v82
	v_exp_f32_e32 v81, v84
	v_exp_f32_e32 v82, v85
	v_exp_f32_e32 v83, v86
	v_exp_f32_e32 v84, v87
	v_exp_f32_e32 v44, v88
	v_exp_f32_e32 v45, v89
	v_exp_f32_e32 v46, v90
	v_exp_f32_e32 v47, v91
	v_exp_f32_e32 v48, v92
	v_exp_f32_e32 v49, v93
	v_exp_f32_e32 v50, v94
	v_exp_f32_e32 v51, v95
	v_exp_f32_e32 v75, v96
	v_exp_f32_e32 v85, v97
	v_exp_f32_e32 v86, v98
	v_exp_f32_e32 v87, v99
	v_exp_f32_e32 v88, v100
	v_exp_f32_e32 v89, v101
	v_exp_f32_e32 v90, v102
	v_exp_f32_e32 v91, v103
	v_mov_b32_e32 v72, 0
	v_mov_b32_e32 v76, 0
	v_mov_b32_e32 v73, 0
	v_mov_b32_e32 v77, 0
	v_cvt_pk_fp8_f32 v72, v36, v37
	v_cvt_pk_fp8_f32 v76, v44, v45
	v_cvt_pk_fp8_f32 v73, v40, v41
	v_cvt_pk_fp8_f32 v77, v48, v49
	v_cvt_pk_fp8_f32 v72, v38, v39 op_sel:[0,0,1]
	v_cvt_pk_fp8_f32 v76, v46, v47 op_sel:[0,0,1]
	v_cvt_pk_fp8_f32 v73, v42, v43 op_sel:[0,0,1]
	v_cvt_pk_fp8_f32 v77, v50, v51 op_sel:[0,0,1]
	v_mfma_f32_16x16x128_f8f6f4 v[200:203], v[124:131], v[148:155], v[200:203]
	v_mov_b32_e32 v78, 0
	v_mov_b32_e32 v79, 0
	v_mov_b32_e32 v74, 0
	v_cvt_pk_fp8_f32 v78, v75, v85
	v_mov_b32_e32 v75, 0
	v_cvt_pk_fp8_f32 v74, v53, v54
	v_cvt_pk_fp8_f32 v75, v81, v82
	v_cvt_pk_fp8_f32 v79, v88, v89
	v_cvt_pk_fp8_f32 v78, v86, v87 op_sel:[0,0,1]
	v_cvt_pk_fp8_f32 v74, v55, v80 op_sel:[0,0,1]
	v_cvt_pk_fp8_f32 v75, v83, v84 op_sel:[0,0,1]
	v_cvt_pk_fp8_f32 v79, v90, v91 op_sel:[0,0,1]
	ds_read_b128 v[80:83], v113 offset:16384
	s_nop 1
	ds_read_b128 v[58:61], v113 offset:16896
	ds_read_b128 v[84:87], v113 offset:17408
	ds_read_b128 v[62:65], v113 offset:17920
	s_mov_b32 s12, 0x43c80000
	v_mfma_f32_16x16x128_f8f6f4 v[200:203], v[124:131], v[72:79], v[200:203]
	s_nop 15
	s_nop 3
	v_sub_f32_e32 v37, v200, v204
	v_max3_f32 v0, v0, v52, v37
	v_cmp_nge_f32_e32 vcc, s12, v0
	s_cmp_lg_u64 vcc, 0
	s_cselect_b64 s[12:13], -1, 0
	s_cbranch_vccz .LBB1_12
	v_mfma_f32_32x32x64_f8f6f4 v[4:19], v[104:111], v[132:139], v[4:19]
	s_andn2_b64 vcc, exec, s[12:13]
	v_mfma_f32_32x32x64_f8f6f4 v[20:35], v[140:147], v[132:139], v[20:35]
	s_cbranch_vccnz .LBB1_5
